# baseline (speedup 1.0000x reference)
.Lmy_proj_noprio:
	s_load_dwordx4 s[4:7], s[0:1], 0x20
	s_load_dwordx2 s[12:13], s[0:1], 0x30
	v_and_b32_e32 v73, 63, v0
	v_and_b32_e32 v1, 31, v0
	v_lshrrev_b32_e32 v76, 6, v0
	v_bfe_u32 v77, v0, 5, 1
	v_or_b32_e32 v45, 0x200, v0
	v_or_b32_e32 v46, 0x600, v0
	v_or_b32_e32 v47, 0xa00, v0
	v_or_b32_e32 v48, 0xe00, v0
	v_lshlrev_b32_e32 v34, 15, v76
	v_mov_b32_e32 v35, v71
	v_lshl_add_u64 v[34:35], s[8:9], 0, v[34:35]
	v_lshlrev_b32_e32 v36, 4, v73
	v_mov_b32_e32 v37, v71
	v_lshl_add_u64 v[68:69], v[34:35], 0, v[36:37]
	s_movk_i32 s0, 0x5000
	v_add_co_u32_e32 v38, vcc, s0, v68
	s_movk_i32 s0, 0x4000
	s_nop 0
	v_addc_co_u32_e32 v39, vcc, 0, v69, vcc
	global_load_dwordx4 v[34:37], v[68:69], off
	global_load_dwordx4 v[78:81], v[38:39], off offset:-4096
	v_add_co_u32_e32 v40, vcc, s0, v68
	s_nop 1
	v_addc_co_u32_e32 v41, vcc, 0, v69, vcc
	global_load_dwordx4 v[82:85], v[68:69], off offset:1024
	global_load_dwordx4 v[86:89], v[40:41], off offset:1024
	global_load_dwordx4 v[90:93], v[68:69], off offset:2048
	global_load_dwordx4 v[94:97], v[40:41], off offset:2048
	global_load_dwordx4 v[98:101], v[68:69], off offset:3072
	global_load_dwordx4 v[102:105], v[40:41], off offset:3072
	v_add_co_u32_e32 v74, vcc, s14, v68
	s_movk_i32 s0, 0x1000
	s_nop 0
	v_addc_co_u32_e32 v75, vcc, 0, v69, vcc
	global_load_dwordx4 v[106:109], v[74:75], off offset:-4096
	global_load_dwordx4 v[110:113], v[38:39], off
	v_add_co_u32_e32 v40, vcc, s0, v68
	s_nop 1
	v_addc_co_u32_e32 v41, vcc, 0, v69, vcc
	global_load_dwordx4 v[114:117], v[40:41], off offset:1024
	global_load_dwordx4 v[118:121], v[38:39], off offset:1024
	global_load_dwordx4 v[122:125], v[40:41], off offset:2048
	global_load_dwordx4 v[126:129], v[38:39], off offset:2048
	global_load_dwordx4 v[130:133], v[40:41], off offset:3072
	global_load_dwordx4 v[134:137], v[38:39], off offset:3072
	v_lshlrev_b32_e32 v38, 3, v0
	v_and_b32_e32 v38, 0x1f8, v38
	v_add_u32_e32 v38, 0, v38
	s_movk_i32 s0, 0x210
	s_waitcnt vmcnt(17)
	v_cvt_pk_f16_f32 v29, v28, v29
	v_cvt_pk_f16_f32 v28, v26, v27
	v_mad_u32_u24 v26, v76, s0, v38
	ds_write_b64 v26, v[28:29]
	v_lshrrev_b32_e32 v26, 6, v45
	v_cvt_pk_f16_f32 v5, v4, v5
	v_cvt_pk_f16_f32 v4, v2, v3
	v_mad_u32_u24 v2, v26, s0, v38
	ds_write_b64 v2, v[4:5]
	v_lshrrev_b32_e32 v4, 6, v42
	v_cvt_pk_f16_f32 v3, v8, v9
	v_cvt_pk_f16_f32 v2, v6, v7
	v_mad_u32_u24 v4, v4, s0, v38
	ds_write_b64 v4, v[2:3]
	v_lshrrev_b32_e32 v4, 6, v46
	v_cvt_pk_f16_f32 v3, v12, v13
	v_cvt_pk_f16_f32 v2, v10, v11
	v_mad_u32_u24 v4, v4, s0, v38
	ds_write_b64 v4, v[2:3]
	v_lshrrev_b32_e32 v4, 6, v43
	v_cvt_pk_f16_f32 v3, v16, v17
	v_cvt_pk_f16_f32 v2, v14, v15
	v_mad_u32_u24 v4, v4, s0, v38
	ds_write_b64 v4, v[2:3]
	v_lshrrev_b32_e32 v4, 6, v47
	v_cvt_pk_f16_f32 v3, v20, v21
	v_cvt_pk_f16_f32 v2, v18, v19
	v_mad_u32_u24 v4, v4, s0, v38
	ds_write_b64 v4, v[2:3]
	v_lshrrev_b32_e32 v4, 6, v44
	v_cvt_pk_f16_f32 v3, v24, v25
	v_cvt_pk_f16_f32 v2, v22, v23
	v_mad_u32_u24 v4, v4, s0, v38
	ds_write_b64 v4, v[2:3]
	v_lshrrev_b32_e32 v4, 6, v48
	s_waitcnt vmcnt(16)
	v_cvt_pk_f16_f32 v3, v32, v33
	v_cvt_pk_f16_f32 v2, v30, v31
	v_mad_u32_u24 v4, v4, s0, v38
	ds_write_b64 v4, v[2:3]
	v_mul_u32_u24_e32 v2, 0x210, v1
	v_lshlrev_b32_e32 v66, 4, v77
	v_add3_u32 v67, 0, v2, v66
	s_waitcnt lgkmcnt(0)
	s_barrier
	ds_read_b128 v[2:5], v67
	ds_read_b128 v[138:141], v67 offset:32
	ds_read_b128 v[6:9], v67 offset:16896
	ds_read_b128 v[142:145], v67 offset:16928
	s_movk_i32 s0, 0x7000
	v_add_co_u32_e32 v166, vcc, s0, v68
	s_waitcnt vmcnt(15) lgkmcnt(3)
	v_mfma_f32_32x32x16_f16 v[50:65], v[34:37], v[2:5], 0
	v_addc_co_u32_e32 v167, vcc, 0, v69, vcc
	global_load_dwordx4 v[146:149], v[74:75], off
	global_load_dwordx4 v[150:153], v[166:167], off offset:-4096
	ds_read_b128 v[154:157], v67 offset:64
	ds_read_b128 v[158:161], v67 offset:16960
	v_add_co_u32_e32 v168, vcc, s3, v68
	s_waitcnt lgkmcnt(3)
	v_mfma_f32_32x32x16_f16 v[34:49], v[34:37], v[6:9], 0
	v_addc_co_u32_e32 v169, vcc, 0, v69, vcc
	s_waitcnt vmcnt(16)
	v_mfma_f32_32x32x16_f16 v[18:33], v[78:81], v[2:5], 0
	v_mfma_f32_32x32x16_f16 v[2:17], v[78:81], v[6:9], 0
	s_waitcnt vmcnt(15)
	v_mfma_f32_32x32x16_f16 v[50:65], v[82:85], v[138:141], v[50:65]
	s_waitcnt lgkmcnt(2)
	v_mfma_f32_32x32x16_f16 v[34:49], v[82:85], v[142:145], v[34:49]
	global_load_dwordx4 v[78:81], v[74:75], off offset:1024
	global_load_dwordx4 v[82:85], v[168:169], off offset:1024
	s_waitcnt vmcnt(16)
	v_mfma_f32_32x32x16_f16 v[2:17], v[86:89], v[142:145], v[2:17]
	v_mfma_f32_32x32x16_f16 v[18:33], v[86:89], v[138:141], v[18:33]
	ds_read_b128 v[138:141], v67 offset:96
	ds_read_b128 v[162:165], v67 offset:16992
	s_waitcnt vmcnt(15) lgkmcnt(3)
	v_mfma_f32_32x32x16_f16 v[50:65], v[90:93], v[154:157], v[50:65]
	s_waitcnt lgkmcnt(2)
	v_mfma_f32_32x32x16_f16 v[34:49], v[90:93], v[158:161], v[34:49]
	global_load_dwordx4 v[86:89], v[74:75], off offset:2048
	global_load_dwordx4 v[90:93], v[168:169], off offset:2048
	s_waitcnt vmcnt(16)
	v_mfma_f32_32x32x16_f16 v[2:17], v[94:97], v[158:161], v[2:17]
	v_mfma_f32_32x32x16_f16 v[18:33], v[94:97], v[154:157], v[18:33]
	ds_read_b128 v[142:145], v67 offset:128
	ds_read_b128 v[154:157], v67 offset:17024
	s_waitcnt vmcnt(15) lgkmcnt(3)
	v_mfma_f32_32x32x16_f16 v[50:65], v[98:101], v[138:141], v[50:65]
	s_waitcnt lgkmcnt(2)
	v_mfma_f32_32x32x16_f16 v[34:49], v[98:101], v[162:165], v[34:49]
	global_load_dwordx4 v[94:97], v[74:75], off offset:3072
	global_load_dwordx4 v[98:101], v[168:169], off offset:3072
	s_waitcnt vmcnt(16)
	v_mfma_f32_32x32x16_f16 v[2:17], v[102:105], v[162:165], v[2:17]
	v_mfma_f32_32x32x16_f16 v[18:33], v[102:105], v[138:141], v[18:33]
	ds_read_b128 v[138:141], v67 offset:160
	ds_read_b128 v[158:161], v67 offset:17056
	s_movk_i32 s0, 0x3000
	v_add_co_u32_e32 v68, vcc, s0, v68
	s_waitcnt vmcnt(15) lgkmcnt(3)
	v_mfma_f32_32x32x16_f16 v[50:65], v[106:109], v[142:145], v[50:65]
	v_addc_co_u32_e32 v69, vcc, 0, v69, vcc
	s_waitcnt lgkmcnt(2)
	v_mfma_f32_32x32x16_f16 v[34:49], v[106:109], v[154:157], v[34:49]
	global_load_dwordx4 v[102:105], v[68:69], off
	global_load_dwordx4 v[106:109], v[166:167], off
	s_waitcnt vmcnt(16)
	v_mfma_f32_32x32x16_f16 v[2:17], v[110:113], v[154:157], v[2:17]
	v_mfma_f32_32x32x16_f16 v[18:33], v[110:113], v[142:145], v[18:33]
	ds_read_b128 v[142:145], v67 offset:192
	ds_read_b128 v[162:165], v67 offset:17088
	s_waitcnt vmcnt(15) lgkmcnt(3)
	v_mfma_f32_32x32x16_f16 v[50:65], v[114:117], v[138:141], v[50:65]
	s_waitcnt lgkmcnt(2)
	v_mfma_f32_32x32x16_f16 v[34:49], v[114:117], v[158:161], v[34:49]
	global_load_dwordx4 v[110:113], v[68:69], off offset:1024
	global_load_dwordx4 v[114:117], v[166:167], off offset:1024
	s_waitcnt vmcnt(16)
	v_mfma_f32_32x32x16_f16 v[2:17], v[118:121], v[158:161], v[2:17]
	v_mfma_f32_32x32x16_f16 v[18:33], v[118:121], v[138:141], v[18:33]
	ds_read_b128 v[138:141], v67 offset:224
	ds_read_b128 v[154:157], v67 offset:17120
	s_waitcnt vmcnt(15) lgkmcnt(3)
	v_mfma_f32_32x32x16_f16 v[50:65], v[122:125], v[142:145], v[50:65]
	s_waitcnt lgkmcnt(2)
	v_mfma_f32_32x32x16_f16 v[34:49], v[122:125], v[162:165], v[34:49]
	global_load_dwordx4 v[118:121], v[68:69], off offset:2048
	global_load_dwordx4 v[122:125], v[166:167], off offset:2048
	s_waitcnt vmcnt(16)
	v_mfma_f32_32x32x16_f16 v[2:17], v[126:129], v[162:165], v[2:17]
	v_mfma_f32_32x32x16_f16 v[18:33], v[126:129], v[142:145], v[18:33]
	ds_read_b128 v[142:145], v67 offset:256
	ds_read_b128 v[158:161], v67 offset:17152
	s_waitcnt vmcnt(15) lgkmcnt(3)
	v_mfma_f32_32x32x16_f16 v[50:65], v[130:133], v[138:141], v[50:65]
	s_waitcnt lgkmcnt(2)
	v_mfma_f32_32x32x16_f16 v[34:49], v[130:133], v[154:157], v[34:49]
	global_load_dwordx4 v[126:129], v[68:69], off offset:3072
	global_load_dwordx4 v[130:133], v[166:167], off offset:3072
	s_waitcnt vmcnt(16)
	v_mfma_f32_32x32x16_f16 v[2:17], v[134:137], v[154:157], v[2:17]
	v_mfma_f32_32x32x16_f16 v[18:33], v[134:137], v[138:141], v[18:33]
	ds_read_b128 v[138:141], v67 offset:288
	ds_read_b128 v[162:165], v67 offset:17184
	s_waitcnt vmcnt(14) lgkmcnt(2)
	v_mfma_f32_32x32x16_f16 v[2:17], v[150:153], v[158:161], v[2:17]
	v_mfma_f32_32x32x16_f16 v[50:65], v[146:149], v[142:145], v[50:65]
	v_mfma_f32_32x32x16_f16 v[18:33], v[150:153], v[142:145], v[18:33]
	ds_read_b128 v[134:137], v67 offset:320
	ds_read_b128 v[142:145], v67 offset:17216
	v_mfma_f32_32x32x16_f16 v[34:49], v[146:149], v[158:161], v[34:49]
	s_waitcnt vmcnt(12) lgkmcnt(2)
	v_mfma_f32_32x32x16_f16 v[2:17], v[82:85], v[162:165], v[2:17]
	v_mfma_f32_32x32x16_f16 v[50:65], v[78:81], v[138:141], v[50:65]
	v_mfma_f32_32x32x16_f16 v[34:49], v[78:81], v[162:165], v[34:49]
	v_mfma_f32_32x32x16_f16 v[18:33], v[82:85], v[138:141], v[18:33]
	ds_read_b128 v[78:81], v67 offset:352
	ds_read_b128 v[138:141], v67 offset:17248
	s_waitcnt vmcnt(10) lgkmcnt(2)
	v_mfma_f32_32x32x16_f16 v[2:17], v[90:93], v[142:145], v[2:17]
	v_mfma_f32_32x32x16_f16 v[50:65], v[86:89], v[134:137], v[50:65]
	v_mfma_f32_32x32x16_f16 v[34:49], v[86:89], v[142:145], v[34:49]
	ds_read_b128 v[82:85], v67 offset:384
	ds_read_b128 v[86:89], v67 offset:17280
	v_mfma_f32_32x32x16_f16 v[18:33], v[90:93], v[134:137], v[18:33]
	s_waitcnt vmcnt(8) lgkmcnt(2)
	v_mfma_f32_32x32x16_f16 v[2:17], v[98:101], v[138:141], v[2:17]
	v_mfma_f32_32x32x16_f16 v[50:65], v[94:97], v[78:81], v[50:65]
	v_mfma_f32_32x32x16_f16 v[18:33], v[98:101], v[78:81], v[18:33]
	ds_read_b128 v[78:81], v67 offset:416
	ds_read_b128 v[90:93], v67 offset:17312
	v_mfma_f32_32x32x16_f16 v[34:49], v[94:97], v[138:141], v[34:49]
	s_waitcnt vmcnt(6) lgkmcnt(2)
	v_mfma_f32_32x32x16_f16 v[2:17], v[106:109], v[86:89], v[2:17]
	v_mfma_f32_32x32x16_f16 v[50:65], v[102:105], v[82:85], v[50:65]
	v_mfma_f32_32x32x16_f16 v[18:33], v[106:109], v[82:85], v[18:33]
	ds_read_b128 v[82:85], v67 offset:448
	ds_read_b128 v[94:97], v67 offset:17344
	v_mfma_f32_32x32x16_f16 v[34:49], v[102:105], v[86:89], v[34:49]
	s_waitcnt vmcnt(4) lgkmcnt(2)
	v_mfma_f32_32x32x16_f16 v[2:17], v[114:117], v[90:93], v[2:17]
	v_mfma_f32_32x32x16_f16 v[50:65], v[110:113], v[78:81], v[50:65]
	v_mfma_f32_32x32x16_f16 v[18:33], v[114:117], v[78:81], v[18:33]
	ds_read_b128 v[78:81], v67 offset:480
	ds_read_b128 v[86:89], v67 offset:17376
	v_mfma_f32_32x32x16_f16 v[34:49], v[110:113], v[90:93], v[34:49]
	s_waitcnt vmcnt(2) lgkmcnt(2)
	v_mfma_f32_32x32x16_f16 v[2:17], v[122:125], v[94:97], v[2:17]
	v_mfma_f32_32x32x16_f16 v[50:65], v[118:121], v[82:85], v[50:65]
	v_mfma_f32_32x32x16_f16 v[34:49], v[118:121], v[94:97], v[34:49]
	v_mfma_f32_32x32x16_f16 v[18:33], v[122:125], v[82:85], v[18:33]
	s_waitcnt vmcnt(0) lgkmcnt(0)
	v_mfma_f32_32x32x16_f16 v[2:17], v[130:133], v[86:89], v[2:17]
	v_mfma_f32_32x32x16_f16 v[50:65], v[126:129], v[78:81], v[50:65]
	v_mfma_f32_32x32x16_f16 v[34:49], v[126:129], v[86:89], v[34:49]
	v_mfma_f32_32x32x16_f16 v[18:33], v[130:133], v[78:81], v[18:33]
	v_and_b32_e32 v98, 0x1c0, v0
	v_and_b32_e32 v67, 0xc0, v0
	v_lshlrev_b32_e32 v74, 2, v98
	v_mov_b32_e32 v75, v71
	s_movk_i32 s0, 0xfc00
	s_movk_i32 s3, 0x100
	v_lshlrev_b32_e32 v68, 2, v67
	v_mov_b32_e32 v69, v71
	v_lshl_add_u64 v[74:75], s[4:5], 0, v[74:75]
	s_mov_b32 s1, -1
	v_lshl_add_u64 v[68:69], s[10:11], 0, v[68:69]
	v_lshl_add_u64 v[74:75], v[74:75], 0, s[0:1]
	v_mov_b32_e32 v67, 0x3ed96d27
	v_cmp_gt_u32_e32 vcc, s3, v0
	s_barrier
	s_nop 0
	v_cndmask_b32_e32 v72, 1.0, v67, vcc
	v_cndmask_b32_e32 v69, v75, v69, vcc
	v_cndmask_b32_e32 v68, v74, v68, vcc
	v_mov_b32_e32 v67, v71
	v_lshl_add_u64 v[74:75], v[68:69], 0, v[66:67]
	global_load_dwordx4 v[66:69], v[74:75], off
	global_load_dwordx4 v[78:81], v[74:75], off offset:32
	global_load_dwordx4 v[82:85], v[74:75], off offset:64
	global_load_dwordx4 v[86:89], v[74:75], off offset:96
	global_load_dwordx4 v[90:93], v[74:75], off offset:128
	global_load_dwordx4 v[94:97], v[74:75], off offset:160
	s_movk_i32 s0, 0x90
	v_mad_u32_u24 v71, v98, s0, 0
	global_load_dwordx4 v[98:101], v[74:75], off offset:192
	global_load_dwordx4 v[102:105], v[74:75], off offset:224
	v_lshlrev_b32_e32 v77, 3, v77
	v_mul_u32_u24_e32 v1, 0x90, v1
	v_add3_u32 v77, v71, v77, v1
	s_movk_i32 s0, 0xff
	v_add_u32_e32 v106, 0x1000, v77
	v_cmp_lt_u32_e64 s[0:1], s0, v0
	s_lshr_b32 s3, s2, 3
	s_and_b32 s3, s3, 0x3ffc
	s_lshl_b32 s2, s2, 13
	s_and_b32 s2, s2, 0x3e000
	s_waitcnt vmcnt(7)
	v_add_f32_e64 v50, v66, v50
	v_add_f32_e64 v51, v67, v51
	v_add_f32_e64 v52, v68, v52
	v_add_f32_e64 v53, v69, v53
	s_waitcnt vmcnt(6)
	v_add_f32_e64 v54, v78, v54
	v_add_f32_e64 v55, v79, v55
	v_add_f32_e64 v56, v80, v56
	v_add_f32_e64 v57, v81, v57
	s_waitcnt vmcnt(3)
	v_add_f32_e64 v18, v90, v18
	v_add_f32_e64 v19, v91, v19
	v_add_f32_e64 v20, v92, v20
	v_add_f32_e64 v21, v93, v21
	v_add_f32_e64 v2, v90, v2
	v_add_f32_e64 v3, v91, v3
	v_add_f32_e64 v4, v92, v4
	v_add_f32_e64 v5, v93, v5
	v_mul_f32_e64 v18, v72, v18
	v_mul_f32_e64 v19, v72, v19
	v_mul_f32_e64 v20, v72, v20
	v_mul_f32_e64 v21, v72, v21
	v_mul_f32_e64 v2, v72, v2
	v_mul_f32_e64 v3, v72, v3
	v_mul_f32_e64 v4, v72, v4
	v_mul_f32_e64 v5, v72, v5
	v_cvt_pk_f16_f32 v18, v18, v19
	v_cvt_pk_f16_f32 v19, v20, v21
	v_cvt_pk_f16_f32 v2, v2, v3
	v_cvt_pk_f16_f32 v3, v4, v5
	s_waitcnt vmcnt(2)
	v_add_f32_e64 v4, v94, v22
	v_add_f32_e64 v5, v95, v23
	v_add_f32_e64 v20, v96, v24
	v_add_f32_e64 v21, v97, v25
	v_add_f32_e64 v58, v82, v58
	v_add_f32_e64 v59, v83, v59
	v_add_f32_e64 v60, v84, v60
	v_add_f32_e64 v61, v85, v61
	v_add_f32_e64 v62, v86, v62
	v_add_f32_e64 v63, v87, v63
	v_add_f32_e64 v64, v88, v64
	v_add_f32_e64 v65, v89, v65
	v_add_f32_e64 v34, v66, v34
	v_add_f32_e64 v35, v67, v35
	v_add_f32_e64 v36, v68, v36
	v_add_f32_e64 v37, v69, v37
	v_add_f32_e64 v38, v78, v38
	v_add_f32_e64 v39, v79, v39
	v_add_f32_e64 v40, v80, v40
	v_add_f32_e64 v41, v81, v41
	v_mul_f32_e64 v50, v72, v50
	v_mul_f32_e64 v51, v72, v51
	v_mul_f32_e64 v52, v72, v52
	v_mul_f32_e64 v53, v72, v53
	v_mul_f32_e64 v54, v72, v54
	v_mul_f32_e64 v55, v72, v55
	v_mul_f32_e64 v56, v72, v56
	v_mul_f32_e64 v57, v72, v57
	v_mul_f32_e64 v4, v72, v4
	v_mul_f32_e64 v5, v72, v5
	v_mul_f32_e64 v20, v72, v20
	v_mul_f32_e64 v21, v72, v21
	v_mul_f32_e64 v34, v72, v34
	v_mul_f32_e64 v35, v72, v35
	v_mul_f32_e64 v36, v72, v36
	v_mul_f32_e64 v37, v72, v37
	v_mul_f32_e64 v38, v72, v38
	v_mul_f32_e64 v39, v72, v39
	v_mul_f32_e64 v40, v72, v40
	v_mul_f32_e64 v41, v72, v41
	v_mul_f32_e64 v58, v72, v58
	v_mul_f32_e64 v59, v72, v59
	v_mul_f32_e64 v60, v72, v60
	v_mul_f32_e64 v61, v72, v61
	v_mul_f32_e64 v62, v72, v62
	v_mul_f32_e64 v63, v72, v63
	v_mul_f32_e64 v64, v72, v64
	v_mul_f32_e64 v65, v72, v65
	v_cvt_pk_f16_f32 v50, v50, v51
	v_cvt_pk_f16_f32 v51, v52, v53
	v_cvt_pk_f16_f32 v52, v54, v55
	v_cvt_pk_f16_f32 v53, v56, v57
	v_cvt_pk_f16_f32 v4, v4, v5
	v_cvt_pk_f16_f32 v5, v20, v21
	v_cvt_pk_f16_f32 v34, v34, v35
	v_cvt_pk_f16_f32 v35, v36, v37
	v_cvt_pk_f16_f32 v36, v38, v39
	v_cvt_pk_f16_f32 v37, v40, v41
	v_cvt_pk_f16_f32 v38, v58, v59
	v_cvt_pk_f16_f32 v39, v60, v61
	v_cvt_pk_f16_f32 v40, v62, v63
	v_cvt_pk_f16_f32 v41, v64, v65
	ds_write2_b64 v77, v[50:51], v[52:53] offset1:2
	ds_write2_b64 v106, v[34:35], v[36:37] offset0:64 offset1:66
	ds_write2_b64 v77, v[38:39], v[40:41] offset0:4 offset1:6
	ds_write2_b64 v77, v[18:19], v[4:5] offset0:8 offset1:10
	v_add_f32_e64 v0, v94, v6
	v_add_f32_e64 v1, v95, v7
	v_add_f32_e64 v4, v96, v8
	v_add_f32_e64 v5, v97, v9
	v_mul_f32_e64 v0, v72, v0
	v_mul_f32_e64 v1, v72, v1
	v_mul_f32_e64 v4, v72, v4
	v_mul_f32_e64 v5, v72, v5
	v_cvt_pk_f16_f32 v0, v0, v1
	v_cvt_pk_f16_f32 v1, v4, v5
	ds_write2_b64 v106, v[2:3], v[0:1] offset0:72 offset1:74
	s_waitcnt vmcnt(1)
	v_add_f32_e64 v0, v98, v26
	v_add_f32_e64 v1, v99, v27
	v_add_f32_e64 v2, v100, v28
	v_add_f32_e64 v3, v101, v29
	v_mul_f32_e64 v0, v72, v0
	v_mul_f32_e64 v1, v72, v1
	v_mul_f32_e64 v2, v72, v2
	v_mul_f32_e64 v3, v72, v3
	v_cvt_pk_f16_f32 v0, v0, v1
	v_cvt_pk_f16_f32 v1, v2, v3
	v_add_f32_e64 v2, v98, v10
	v_add_f32_e64 v3, v99, v11
	v_add_f32_e64 v4, v100, v12
	v_add_f32_e64 v5, v101, v13
	v_mul_f32_e64 v2, v72, v2
	v_mul_f32_e64 v3, v72, v3
	v_mul_f32_e64 v4, v72, v4
	v_mul_f32_e64 v5, v72, v5
	v_cvt_pk_f16_f32 v2, v2, v3
	v_cvt_pk_f16_f32 v3, v4, v5
	s_waitcnt vmcnt(0)
	v_add_f32_e64 v4, v102, v30
	v_add_f32_e64 v5, v103, v31
	v_add_f32_e64 v6, v104, v32
	v_add_f32_e64 v7, v105, v33
	v_mul_f32_e64 v4, v72, v4
	v_mul_f32_e64 v5, v72, v5
	v_mul_f32_e64 v6, v72, v6
	v_mul_f32_e64 v7, v72, v7
	v_cvt_pk_f16_f32 v4, v4, v5
	v_cvt_pk_f16_f32 v5, v6, v7
	ds_write2_b64 v77, v[0:1], v[4:5] offset0:12 offset1:14
	v_add_f32_e64 v0, v102, v14
	v_add_f32_e64 v1, v103, v15
	v_add_f32_e64 v4, v104, v16
	v_add_f32_e64 v5, v105, v17
	v_mul_f32_e64 v0, v72, v0
	v_mul_f32_e64 v1, v72, v1
	v_mul_f32_e64 v4, v72, v4
	v_mul_f32_e64 v5, v72, v5
	v_cvt_pk_f16_f32 v0, v0, v1
	v_cvt_pk_f16_f32 v1, v4, v5
	ds_write2_b64 v106, v[2:3], v[0:1] offset0:76 offset1:78
	v_mov_b32_e32 v0, s12
	v_mov_b32_e32 v1, s6
	v_add_f32_e64 v42, v82, v42
	v_add_f32_e64 v43, v83, v43
	v_add_f32_e64 v44, v84, v44
	v_add_f32_e64 v45, v85, v45
	v_add_f32_e64 v46, v86, v46
	v_add_f32_e64 v47, v87, v47
	v_add_f32_e64 v48, v88, v48
	v_add_f32_e64 v49, v89, v49
	v_cndmask_b32_e32 v0, v0, v1, vcc
	v_mov_b32_e32 v1, s13
	v_mov_b32_e32 v2, s7
	v_and_or_b32 v4, v76, 3, s3
	v_mul_f32_e64 v42, v72, v42
	v_mul_f32_e64 v43, v72, v43
	v_mul_f32_e64 v44, v72, v44
	v_mul_f32_e64 v45, v72, v45
	v_mul_f32_e64 v46, v72, v46
	v_mul_f32_e64 v47, v72, v47
	v_mul_f32_e64 v48, v72, v48
	v_mul_f32_e64 v49, v72, v49
	v_cndmask_b32_e32 v1, v1, v2, vcc
	v_lshl_or_b32 v4, v4, 18, s2
	v_cvt_pk_f16_f32 v42, v42, v43
	v_cvt_pk_f16_f32 v43, v44, v45
	v_cvt_pk_f16_f32 v44, v46, v47
	v_cvt_pk_f16_f32 v45, v48, v49
	v_and_b32_e32 v1, 0xffff, v1
	v_mov_b32_e32 v2, 0x800000
	v_mov_b32_e32 v3, 0x20000
	v_lshl_or_b32 v8, v73, 4, v4
	ds_write2_b64 v106, v[42:43], v[44:45] offset0:68 offset1:70
	s_and_saveexec_b64 s[2:3], s[0:1]
	s_xor_b64 s[2:3], exec, s[2:3]
	s_cbranch_execz .LBB1_18
	v_lshrrev_b32_e32 v4, 2, v73
	v_mul_u32_u24_e32 v4, 0x90, v4
	v_and_b32_e32 v5, 48, v70
	v_add3_u32 v9, v71, v4, v5
	ds_read_b128 v[4:7], v9
	s_mov_b64 s[8:9], exec

.Lmy_ffn_noprio:
	s_lshl_b32 s6, s6, 13
	s_cmp_lg_u32 0, -1
	s_cselect_b32 s7, 0, 0
	s_add_i32 s10, s7, s6
	s_mov_b64 s[6:7], 0x2000
	s_add_i32 s8, s10, 0x13400
	v_lshl_add_u64 v[24:25], v[180:181], 0, s[6:7]
	s_mov_b32 s9, m0
	s_mov_b32 m0, s8
	s_nop 0
	global_load_lds_dwordx4 v[24:25], off
	s_mov_b32 m0, s9
	s_mov_b64 s[8:9], 0xa000
	v_lshl_add_u64 v[24:25], v[180:181], 0, s[8:9]
	s_add_i32 s8, s10, 0x13800
	s_mov_b32 s9, m0
	s_mov_b32 m0, s8
	s_nop 0
	global_load_lds_dwordx4 v[24:25], off
	s_mov_b32 m0, s9
	s_mov_b64 s[8:9], 0x2400
	s_add_i32 s11, s10, 0x13c00
	v_lshl_add_u64 v[24:25], v[180:181], 0, s[8:9]
	s_mov_b32 s8, m0
	s_mov_b32 m0, s11
	s_nop 0
	global_load_lds_dwordx4 v[24:25], off
	s_mov_b32 m0, s8
	s_mov_b64 s[8:9], 0xa400
	v_lshl_add_u64 v[24:25], v[180:181], 0, s[8:9]
	s_add_i32 s8, s10, 0x14000
	s_mov_b32 s9, m0
	s_mov_b32 m0, s8
	s_nop 0
	global_load_lds_dwordx4 v[24:25], off
	s_mov_b32 m0, s9
	s_mov_b64 s[8:9], 0x2800
	s_add_i32 s11, s10, 0x14400
	v_lshl_add_u64 v[24:25], v[180:181], 0, s[8:9]
	s_mov_b32 s8, m0
	s_mov_b32 m0, s11
	s_nop 0
	global_load_lds_dwordx4 v[24:25], off
	s_mov_b32 m0, s8
	s_mov_b64 s[8:9], 0xa800
	v_lshl_add_u64 v[24:25], v[180:181], 0, s[8:9]
	s_add_i32 s8, s10, 0x14800
	s_mov_b32 s9, m0
	s_mov_b32 m0, s8
	s_nop 0
	global_load_lds_dwordx4 v[24:25], off
	s_mov_b32 m0, s9
	s_mov_b64 s[8:9], 0x2c00
	s_add_i32 s11, s10, 0x14c00
	v_lshl_add_u64 v[24:25], v[180:181], 0, s[8:9]
	s_mov_b32 s8, m0
	s_mov_b32 m0, s11
	s_nop 0
	global_load_lds_dwordx4 v[24:25], off
	s_mov_b32 m0, s8
	s_mov_b64 s[8:9], 0xac00
	v_lshl_add_u64 v[24:25], v[180:181], 0, s[8:9]
	s_add_i32 s9, 0, 0x11400
	v_lshl_add_u32 v19, v37, 2, s9
	s_add_i32 s10, s10, 0x15000
	s_mov_b32 s8, m0
	s_mov_b32 m0, s10
	s_nop 0
	global_load_lds_dwordx4 v[24:25], off
	s_mov_b32 m0, s8
	s_waitcnt vmcnt(8)
	ds_write_b128 v19, v[20:23]
	v_lshrrev_b32_e32 v19, 5, v0
	v_mul_u32_u24_e32 v19, 0x410, v19
	v_and_b32_e32 v18, 0x1f0, v18
	v_add3_u32 v19, 0, v19, v18
	ds_write_b128 v19, v[14:17] offset:512
	v_lshrrev_b32_e32 v14, 5, v186
	v_mul_u32_u24_e32 v14, 0x410, v14
	v_add3_u32 v14, 0, v14, v18
	ds_write_b128 v14, v[6:9] offset:512
	v_lshrrev_b32_e32 v6, 5, v182
	v_mul_u32_u24_e32 v6, 0x410, v6
	v_add3_u32 v6, 0, v6, v18
	s_movk_i32 s10, 0x410
	ds_write_b128 v6, v[2:5] offset:512
	v_lshrrev_b32_e32 v2, 5, v185
	v_mul_u32_u24_e32 v2, 0x410, v2
	v_mad_u32_u24 v189, v205, s10, 0
	v_add3_u32 v2, 0, v2, v18
	v_lshl_add_u32 v202, v208, 4, v189
	ds_write_b128 v2, v[10:13] offset:512
	s_waitcnt lgkmcnt(0)
	s_barrier
	ds_read_b128 v[2:5], v202 offset:512
	ds_read_b128 v[102:105], v202 offset:544
	ds_read_b128 v[6:9], v202 offset:33792
	ds_read_b128 v[106:109], v202 offset:33824
	v_mul_u32_u24_e32 v187, 0x410, v205
	global_load_dwordx4 v[110:113], v[128:129], off
	s_waitcnt vmcnt(8) lgkmcnt(3)
	v_mfma_f32_32x32x16_f16 v[18:33], v[38:41], v[2:5], 0
	ds_read_b128 v[114:117], v202 offset:576
	ds_read_b128 v[118:121], v202 offset:33856
	s_waitcnt lgkmcnt(3)
	v_mfma_f32_32x32x16_f16 v[2:17], v[38:41], v[6:9], 0
	global_load_dwordx4 v[38:41], v[128:129], off offset:1024
	s_waitcnt vmcnt(8)
	v_mfma_f32_32x32x16_f16 v[18:33], v[42:45], v[102:105], v[18:33]
	ds_read_b128 v[102:105], v202 offset:608
	ds_read_b128 v[122:125], v202 offset:33888
	s_waitcnt lgkmcnt(4)
	v_mfma_f32_32x32x16_f16 v[2:17], v[42:45], v[106:109], v[2:17]
	global_load_dwordx4 v[42:45], v[128:129], off offset:2048
	s_waitcnt vmcnt(8) lgkmcnt(3)
	v_mfma_f32_32x32x16_f16 v[18:33], v[46:49], v[114:117], v[18:33]
	ds_read_b128 v[106:109], v202 offset:640
	ds_read_b128 v[114:117], v202 offset:33920
	s_waitcnt lgkmcnt(4)
	v_mfma_f32_32x32x16_f16 v[2:17], v[46:49], v[118:121], v[2:17]
	global_load_dwordx4 v[46:49], v[128:129], off offset:3072
	s_waitcnt vmcnt(8) lgkmcnt(3)
	v_mfma_f32_32x32x16_f16 v[18:33], v[50:53], v[102:105], v[18:33]
	ds_read_b128 v[102:105], v202 offset:672
	ds_read_b128 v[118:121], v202 offset:33952
	s_waitcnt lgkmcnt(4)
	v_mfma_f32_32x32x16_f16 v[2:17], v[50:53], v[122:125], v[2:17]
	s_movk_i32 s8, 0x3000
	v_add_co_u32_e32 v126, vcc, s8, v126
	s_waitcnt vmcnt(7) lgkmcnt(3)
	v_mfma_f32_32x32x16_f16 v[18:33], v[54:57], v[106:109], v[18:33]
	v_addc_co_u32_e32 v127, vcc, 0, v127, vcc
	global_load_dwordx4 v[50:53], v[126:127], off
	ds_read_b128 v[106:109], v202 offset:704
	ds_read_b128 v[122:125], v202 offset:33984
	s_waitcnt lgkmcnt(4)
	v_mfma_f32_32x32x16_f16 v[2:17], v[54:57], v[114:117], v[2:17]
	global_load_dwordx4 v[54:57], v[126:127], off offset:1024
	s_waitcnt vmcnt(8) lgkmcnt(3)
	v_mfma_f32_32x32x16_f16 v[18:33], v[58:61], v[102:105], v[18:33]
	ds_read_b128 v[102:105], v202 offset:736
	ds_read_b128 v[114:117], v202 offset:34016
	s_waitcnt lgkmcnt(4)
	v_mfma_f32_32x32x16_f16 v[2:17], v[58:61], v[118:121], v[2:17]
	global_load_dwordx4 v[58:61], v[126:127], off offset:2048
	s_waitcnt vmcnt(8) lgkmcnt(3)
	v_mfma_f32_32x32x16_f16 v[18:33], v[62:65], v[106:109], v[18:33]
	ds_read_b128 v[106:109], v202 offset:768
	ds_read_b128 v[118:121], v202 offset:34048
	s_waitcnt lgkmcnt(4)
	v_mfma_f32_32x32x16_f16 v[2:17], v[62:65], v[122:125], v[2:17]
	global_load_dwordx4 v[62:65], v[126:127], off offset:3072
	s_waitcnt vmcnt(8) lgkmcnt(3)
	v_mfma_f32_32x32x16_f16 v[18:33], v[98:101], v[102:105], v[18:33]
	ds_read_b128 v[102:105], v202 offset:800
	ds_read_b128 v[122:125], v202 offset:34080
	s_waitcnt lgkmcnt(4)
	v_mfma_f32_32x32x16_f16 v[2:17], v[98:101], v[114:117], v[2:17]
	s_waitcnt vmcnt(7) lgkmcnt(3)
	v_mfma_f32_32x32x16_f16 v[18:33], v[110:113], v[106:109], v[18:33]
	ds_read_b128 v[98:101], v202 offset:832
	ds_read_b128 v[106:109], v202 offset:34112
	s_waitcnt lgkmcnt(4)
	v_mfma_f32_32x32x16_f16 v[2:17], v[110:113], v[118:121], v[2:17]
	s_waitcnt vmcnt(6) lgkmcnt(3)
	v_mfma_f32_32x32x16_f16 v[18:33], v[38:41], v[102:105], v[18:33]
	ds_read_b128 v[102:105], v202 offset:864
	ds_read_b128 v[110:113], v202 offset:34144
	s_waitcnt lgkmcnt(4)
	v_mfma_f32_32x32x16_f16 v[2:17], v[38:41], v[122:125], v[2:17]
	s_waitcnt vmcnt(5) lgkmcnt(3)
	v_mfma_f32_32x32x16_f16 v[18:33], v[42:45], v[98:101], v[18:33]
	ds_read_b128 v[38:41], v202 offset:896
	ds_read_b128 v[98:101], v202 offset:34176
	s_waitcnt lgkmcnt(4)
	v_mfma_f32_32x32x16_f16 v[2:17], v[42:45], v[106:109], v[2:17]
	s_waitcnt vmcnt(4) lgkmcnt(3)
	v_mfma_f32_32x32x16_f16 v[18:33], v[46:49], v[102:105], v[18:33]
	ds_read_b128 v[42:45], v202 offset:928
	ds_read_b128 v[102:105], v202 offset:34208
	s_waitcnt lgkmcnt(4)
	v_mfma_f32_32x32x16_f16 v[2:17], v[46:49], v[110:113], v[2:17]
	s_waitcnt vmcnt(3) lgkmcnt(3)
	v_mfma_f32_32x32x16_f16 v[18:33], v[50:53], v[38:41], v[18:33]
	ds_read_b128 v[38:41], v202 offset:960
	ds_read_b128 v[46:49], v202 offset:34240
	s_waitcnt lgkmcnt(4)
	v_mfma_f32_32x32x16_f16 v[2:17], v[50:53], v[98:101], v[2:17]
	s_waitcnt vmcnt(2) lgkmcnt(3)
	v_mfma_f32_32x32x16_f16 v[18:33], v[54:57], v[42:45], v[18:33]
	ds_read_b128 v[42:45], v202 offset:992
	ds_read_b128 v[50:53], v202 offset:34272
	s_waitcnt lgkmcnt(4)
	v_mfma_f32_32x32x16_f16 v[2:17], v[54:57], v[102:105], v[2:17]
	s_waitcnt vmcnt(1) lgkmcnt(3)
	v_mfma_f32_32x32x16_f16 v[18:33], v[58:61], v[38:41], v[18:33]
	s_waitcnt lgkmcnt(2)
	v_mfma_f32_32x32x16_f16 v[2:17], v[58:61], v[46:49], v[2:17]
	s_waitcnt vmcnt(0) lgkmcnt(1)
	v_mfma_f32_32x32x16_f16 v[18:33], v[62:65], v[42:45], v[18:33]
	s_waitcnt lgkmcnt(0)
	v_mfma_f32_32x32x16_f16 v[2:17], v[62:65], v[50:53], v[2:17]
	v_and_b32_e32 v188, 0xfc, v37
	v_lshl_add_u32 v35, v188, 1, 0
	v_cvt_pk_f16_f32 v39, v92, v93
	v_cvt_pk_f16_f32 v38, v90, v91
	v_mad_u32_u24 v37, v209, s10, v35
	ds_write_b64 v37, v[38:39]
	v_lshrrev_b32_e32 v37, 6, v186
	v_cvt_pk_f16_f32 v39, v96, v97
	v_cvt_pk_f16_f32 v38, v94, v95
	v_mad_u32_u24 v40, v37, s10, v35
	v_lshrrev_b32_e32 v44, 6, v182
	ds_write_b64 v40, v[38:39]
	v_cvt_pk_f16_f32 v39, v88, v89
	v_cvt_pk_f16_f32 v38, v86, v87
	v_mad_u32_u24 v40, v44, s10, v35
	v_lshrrev_b32_e32 v45, 6, v185
	ds_write_b64 v40, v[38:39]
	v_cvt_pk_f16_f32 v39, v84, v85
	v_cvt_pk_f16_f32 v38, v82, v83
	v_mad_u32_u24 v40, v45, s10, v35
	v_lshrrev_b32_e32 v46, 6, v179
	ds_write_b64 v40, v[38:39]
	v_cvt_pk_f16_f32 v39, v80, v81
	v_cvt_pk_f16_f32 v38, v78, v79
	v_mad_u32_u24 v40, v46, s10, v35
	v_lshrrev_b32_e32 v47, 6, v184
	ds_write_b64 v40, v[38:39]
	v_cvt_pk_f16_f32 v39, v76, v77
	v_cvt_pk_f16_f32 v38, v74, v75
	v_mad_u32_u24 v40, v47, s10, v35
	v_lshrrev_b32_e32 v48, 6, v1
	ds_write_b64 v40, v[38:39]
	v_cvt_pk_f16_f32 v39, v72, v73
	v_cvt_pk_f16_f32 v38, v70, v71
	v_mad_u32_u24 v40, v48, s10, v35
	v_lshrrev_b32_e32 v49, 6, v183
	v_lshlrev_b32_e32 v207, 2, v208
	ds_write_b64 v40, v[38:39]
	v_cvt_pk_f16_f32 v39, v68, v69
	v_cvt_pk_f16_f32 v38, v66, v67
	v_mad_u32_u24 v35, v49, s10, v35
	v_lshl_or_b32 v191, v209, 5, v207
	ds_write_b64 v35, v[38:39]
	v_lshl_add_u32 v35, v191, 2, s9
	s_waitcnt lgkmcnt(0)
	s_barrier
	ds_read_b128 v[38:41], v35
	v_or_b32_e32 v194, 8, v191
	s_mov_b32 s15, 0x9000
	v_or_b32_e32 v200, 16, v191
	v_or_b32_e32 v201, 24, v191
	s_waitcnt lgkmcnt(0)
	v_add_f32_e32 v18, v38, v18
	v_cvt_f16_f32_e32 v35, v18
	v_mov_b32_e32 v18, v19
	v_mov_b32_e32 v19, v20
	v_add_f32_e32 v20, v41, v21
	v_cvt_f16_f32_e32 v20, v20
	v_mov_b32_e32 v42, v39
	v_mov_b32_e32 v43, v40
	v_add_f32_e64 v18, v42, v18
	v_add_f32_e64 v19, v43, v19
	v_add_f32_e32 v2, v38, v2
	v_cvt_pk_f16_f32 v19, v18, v19
	v_pack_b32_f16 v18, v35, v19
	v_alignbit_b32 v19, v20, v19, 16
	v_lshl_add_u32 v35, v191, 1, v189
	ds_write_b64 v35, v[18:19] offset:512
	v_cvt_f16_f32_e32 v18, v2
	v_mov_b32_e32 v2, v3
	v_mov_b32_e32 v3, v4
	v_add_f32_e32 v4, v41, v5
	v_cvt_f16_f32_e32 v4, v4
	v_add_f32_e64 v2, v42, v2
	v_add_f32_e64 v3, v43, v3
	v_mov_b32_e32 v19, v24
	v_cvt_pk_f16_f32 v3, v2, v3
	v_pack_b32_f16 v2, v18, v3
	v_alignbit_b32 v3, v4, v3, 16
	ds_write_b64 v35, v[2:3] offset:33792
	v_lshl_add_u32 v2, v194, 2, s9
	ds_read_b128 v[2:5], v2
	v_add_co_u32_e32 v24, vcc, s15, v180
	v_mul_u32_u24_e32 v199, 0x410, v209
	v_mul_u32_u24_e32 v198, 0x410, v37
	s_waitcnt lgkmcnt(0)
	v_add_f32_e32 v18, v2, v22
	v_cvt_f16_f32_e32 v20, v18
	v_mov_b32_e32 v38, v3
	v_mov_b32_e32 v39, v4
	v_mov_b32_e32 v18, v23
	v_add_f32_e64 v18, v38, v18
	v_add_f32_e64 v19, v39, v19
	v_add_f32_e32 v3, v5, v25
	v_cvt_pk_f16_f32 v4, v18, v19
	v_addc_co_u32_e32 v25, vcc, 0, v181, vcc
	v_pack_b32_f16 v22, v20, v4
	global_load_dwordx4 v[18:21], v[180:181], off
	global_load_dwordx4 v[102:105], v[24:25], off offset:-4096
	v_cvt_f16_f32_e32 v3, v3
	v_add_f32_e32 v2, v2, v6
	v_add_f32_e32 v5, v5, v9
	v_cvt_f16_f32_e32 v5, v5
	v_alignbit_b32 v23, v3, v4, 16
	v_cvt_f16_f32_e32 v4, v2
	v_mov_b32_e32 v2, v7
	v_mov_b32_e32 v3, v8
	v_add_f32_e64 v2, v38, v2
	v_add_f32_e64 v3, v39, v3
	ds_write_b64 v35, v[22:23] offset:528
	v_cvt_pk_f16_f32 v3, v2, v3
	v_pack_b32_f16 v2, v4, v3
	v_alignbit_b32 v3, v5, v3, 16
	ds_write_b64 v35, v[2:3] offset:33808
	v_lshl_add_u32 v2, v200, 2, s9
	ds_read_b128 v[2:5], v2
	v_mov_b32_e32 v8, v27
	v_mov_b32_e32 v9, v28
	v_mul_u32_u24_e32 v197, 0x410, v44
	v_mul_u32_u24_e32 v195, 0x410, v45
	s_waitcnt lgkmcnt(0)
	v_add_f32_e32 v6, v2, v26
	v_cvt_f16_f32_e32 v22, v6
	v_mov_b32_e32 v6, v3
	v_add_f32_e32 v3, v5, v29
	v_cvt_f16_f32_e32 v3, v3
	v_mov_b32_e32 v7, v4
	v_add_f32_e64 v8, v6, v8
	v_add_f32_e64 v9, v7, v9
	v_add_f32_e32 v2, v2, v10
	v_cvt_pk_f16_f32 v4, v8, v9
	v_add_f32_e32 v5, v5, v13
	v_pack_b32_f16 v8, v22, v4
	v_alignbit_b32 v9, v3, v4, 16
	v_cvt_f16_f32_e32 v4, v2
	v_cvt_f16_f32_e32 v5, v5
	v_mov_b32_e32 v2, v11
	v_mov_b32_e32 v3, v12
	v_add_f32_e64 v2, v6, v2
	v_add_f32_e64 v3, v7, v3
	ds_write_b64 v35, v[8:9] offset:544
	v_cvt_pk_f16_f32 v3, v2, v3
	v_pack_b32_f16 v2, v4, v3
	v_alignbit_b32 v3, v5, v3, 16
	ds_write_b64 v35, v[2:3] offset:33824
	v_lshl_add_u32 v2, v201, 2, s9
	ds_read_b128 v[2:5], v2
	v_mov_b32_e32 v8, v31
	v_mov_b32_e32 v9, v32
	s_mov_b32 s9, 0x8000
	v_mul_u32_u24_e32 v196, 0x410, v46
	s_waitcnt lgkmcnt(0)
	v_add_f32_e32 v6, v2, v30
	v_cvt_f16_f32_e32 v10, v6
	v_mov_b32_e32 v6, v3
	v_add_f32_e32 v3, v5, v33
	v_cvt_f16_f32_e32 v3, v3
	v_mov_b32_e32 v7, v4
	v_add_f32_e64 v8, v6, v8
	v_add_f32_e64 v9, v7, v9
	v_add_f32_e32 v2, v2, v14
	v_cvt_pk_f16_f32 v4, v8, v9
	v_add_f32_e32 v5, v5, v17
	v_pack_b32_f16 v8, v10, v4
	v_alignbit_b32 v9, v3, v4, 16
	v_cvt_f16_f32_e32 v4, v2
	v_cvt_f16_f32_e32 v5, v5
	v_mov_b32_e32 v2, v15
	v_mov_b32_e32 v3, v16
	v_add_f32_e64 v2, v6, v2
	v_add_f32_e64 v3, v7, v3
	v_mul_u32_u24_e32 v193, 0x410, v47
	v_cvt_pk_f16_f32 v3, v2, v3
	v_pack_b32_f16 v2, v4, v3
	v_alignbit_b32 v3, v5, v3, 16
	ds_write_b64 v35, v[2:3] offset:33840
	v_add_co_u32_e32 v2, vcc, s9, v180
	v_mul_u32_u24_e32 v192, 0x410, v48
	v_mul_u32_u24_e32 v190, 0x410, v49
	v_addc_co_u32_e32 v3, vcc, 0, v181, vcc
	ds_write_b64 v35, v[8:9] offset:560
	global_load_dwordx4 v[106:109], v[180:181], off offset:1024
	global_load_dwordx4 v[110:113], v[2:3], off offset:1024
	global_load_dwordx4 v[122:125], v[180:181], off offset:2048
	global_load_dwordx4 v[126:129], v[2:3], off offset:2048
	global_load_dwordx4 v[130:133], v[180:181], off offset:3072
	global_load_dwordx4 v[134:137], v[2:3], off offset:3072
	v_add_co_u32_e32 v2, vcc, s3, v180
	s_nop 1
	v_addc_co_u32_e32 v3, vcc, 0, v181, vcc
	global_load_dwordx4 v[138:141], v[2:3], off
	global_load_dwordx4 v[142:145], v[24:25], off
	global_load_dwordx4 v[150:153], v[2:3], off offset:1024
	global_load_dwordx4 v[154:157], v[24:25], off offset:1024
	global_load_dwordx4 v[158:161], v[2:3], off offset:2048
	global_load_dwordx4 v[162:165], v[24:25], off offset:2048
	global_load_dwordx4 v[166:169], v[2:3], off offset:3072
	global_load_dwordx4 v[210:213], v[24:25], off offset:3072
	s_waitcnt lgkmcnt(0)
	s_barrier
	ds_read_b128 v[2:5], v202
	ds_read_b128 v[114:117], v202 offset:32
	ds_read_b128 v[6:9], v202 offset:33280
	ds_read_b128 v[146:149], v202 offset:33312
	s_add_i32 s9, 0, 0x13400
	v_add3_u32 v204, s9, v36, v34
	s_waitcnt vmcnt(15) lgkmcnt(3)
	v_mfma_f32_32x32x16_f16 v[50:65], v[18:21], v[2:5], 0
	ds_read_b128 v[170:173], v202 offset:64
	ds_read_b128 v[174:177], v202 offset:33344
	ds_read_b128 v[118:121], v204
	ds_read_b128 v[98:101], v204 offset:1024
	s_waitcnt lgkmcnt(5)
	v_mfma_f32_32x32x16_f16 v[34:49], v[18:21], v[6:9], 0
	s_waitcnt vmcnt(14)
	v_mfma_f32_32x32x16_f16 v[18:33], v[102:105], v[2:5], 0
	v_mfma_f32_32x32x16_f16 v[2:17], v[102:105], v[6:9], 0
	s_waitcnt vmcnt(13)
	v_mfma_f32_32x32x16_f16 v[50:65], v[106:109], v[114:117], v[50:65]
	s_waitcnt lgkmcnt(4)
	v_mfma_f32_32x32x16_f16 v[34:49], v[106:109], v[146:149], v[34:49]
	s_waitcnt vmcnt(12)
	v_mfma_f32_32x32x16_f16 v[18:33], v[110:113], v[114:117], v[18:33]
	ds_read_b128 v[214:217], v202 offset:96
	ds_read_b128 v[218:221], v202 offset:33376
	ds_read_b128 v[114:117], v204 offset:2048
	ds_read_b128 v[102:105], v204 offset:3072
	v_mfma_f32_32x32x16_f16 v[2:17], v[110:113], v[146:149], v[2:17]
	s_waitcnt vmcnt(11) lgkmcnt(7)
	v_mfma_f32_32x32x16_f16 v[50:65], v[122:125], v[170:173], v[50:65]
	s_waitcnt lgkmcnt(6)
	v_mfma_f32_32x32x16_f16 v[34:49], v[122:125], v[174:177], v[34:49]
	s_waitcnt vmcnt(10)
	v_mfma_f32_32x32x16_f16 v[18:33], v[126:129], v[170:173], v[18:33]
	ds_read_b128 v[146:149], v202 offset:128
	ds_read_b128 v[170:173], v202 offset:33408
	ds_read_b128 v[122:125], v204 offset:4096
	ds_read_b128 v[106:109], v204 offset:5120
	v_mfma_f32_32x32x16_f16 v[2:17], v[126:129], v[174:177], v[2:17]
	s_waitcnt vmcnt(9) lgkmcnt(7)
	v_mfma_f32_32x32x16_f16 v[50:65], v[130:133], v[214:217], v[50:65]
	s_waitcnt lgkmcnt(6)
	v_mfma_f32_32x32x16_f16 v[34:49], v[130:133], v[218:221], v[34:49]
	ds_read_b128 v[130:133], v202 offset:160
	ds_read_b128 v[174:177], v202 offset:33440
	ds_read_b128 v[126:129], v204 offset:6144
	ds_read_b128 v[110:113], v204 offset:7168
	s_waitcnt vmcnt(8)
	v_mfma_f32_32x32x16_f16 v[18:33], v[134:137], v[214:217], v[18:33]
	v_mfma_f32_32x32x16_f16 v[2:17], v[134:137], v[218:221], v[2:17]
	v_add_co_u32_e32 v226, vcc, s8, v180
	s_mov_b32 s8, 0xb000
	s_nop 0
	v_addc_co_u32_e32 v227, vcc, 0, v181, vcc
	v_add_co_u32_e32 v228, vcc, s8, v180
	s_waitcnt vmcnt(7) lgkmcnt(7)
	v_mfma_f32_32x32x16_f16 v[50:65], v[138:141], v[146:149], v[50:65]
	v_addc_co_u32_e32 v229, vcc, 0, v181, vcc
	s_waitcnt vmcnt(6)
	v_mfma_f32_32x32x16_f16 v[18:33], v[142:145], v[146:149], v[18:33]
	global_load_dwordx4 v[146:149], v[226:227], off
	global_load_dwordx4 v[134:137], v[228:229], off
	s_waitcnt lgkmcnt(6)
	v_mfma_f32_32x32x16_f16 v[34:49], v[138:141], v[170:173], v[34:49]
	ds_read_b128 v[138:141], v202 offset:192
	ds_read_b128 v[214:217], v202 offset:33472
	v_mfma_f32_32x32x16_f16 v[2:17], v[142:145], v[170:173], v[2:17]
	s_waitcnt vmcnt(7) lgkmcnt(5)
	v_mfma_f32_32x32x16_f16 v[50:65], v[150:153], v[130:133], v[50:65]
	s_waitcnt vmcnt(6)
	v_mfma_f32_32x32x16_f16 v[18:33], v[154:157], v[130:133], v[18:33]
	global_load_dwordx4 v[142:145], v[226:227], off offset:1024
	global_load_dwordx4 v[130:133], v[228:229], off offset:1024
	ds_read_b128 v[218:221], v202 offset:224
	ds_read_b128 v[222:225], v202 offset:33504
	s_waitcnt lgkmcnt(6)
	v_mfma_f32_32x32x16_f16 v[34:49], v[150:153], v[174:177], v[34:49]
	v_mfma_f32_32x32x16_f16 v[2:17], v[154:157], v[174:177], v[2:17]
	s_waitcnt vmcnt(7) lgkmcnt(3)
	v_mfma_f32_32x32x16_f16 v[50:65], v[158:161], v[138:141], v[50:65]
	s_waitcnt vmcnt(6)
	v_mfma_f32_32x32x16_f16 v[18:33], v[162:165], v[138:141], v[18:33]
	global_load_dwordx4 v[150:153], v[226:227], off offset:2048
	global_load_dwordx4 v[138:141], v[228:229], off offset:2048
	ds_read_b128 v[174:177], v202 offset:256
	ds_read_b128 v[170:173], v202 offset:33536
	s_waitcnt lgkmcnt(4)
	v_mfma_f32_32x32x16_f16 v[34:49], v[158:161], v[214:217], v[34:49]
	v_mfma_f32_32x32x16_f16 v[2:17], v[162:165], v[214:217], v[2:17]
	global_load_dwordx4 v[158:161], v[226:227], off offset:3072
	global_load_dwordx4 v[154:157], v[228:229], off offset:3072
	s_waitcnt vmcnt(9) lgkmcnt(3)
	v_mfma_f32_32x32x16_f16 v[50:65], v[166:169], v[218:221], v[50:65]
	s_waitcnt lgkmcnt(2)
	v_mfma_f32_32x32x16_f16 v[34:49], v[166:169], v[222:225], v[34:49]
	ds_read_b128 v[166:169], v202 offset:288
	ds_read_b128 v[162:165], v202 offset:33568
	s_waitcnt vmcnt(8)
	v_mfma_f32_32x32x16_f16 v[18:33], v[210:213], v[218:221], v[18:33]
	v_mfma_f32_32x32x16_f16 v[2:17], v[210:213], v[222:225], v[2:17]
	s_mov_b64 s[8:9], 0x4000
	v_add_u32_e32 v203, 0x140, v202
	v_lshl_add_u64 v[180:181], v[180:181], 0, s[8:9]
	s_mov_b64 s[8:9], 0x8000
	s_mov_b64 s[10:11], 0x1000
	s_mov_b64 s[12:13], 0x9000
	v_mov_b32_e32 v210, v203
.LBB3_21:
	v_add_co_u32_e32 v212, vcc, s15, v180
	s_waitcnt vmcnt(15) lgkmcnt(3)
	v_mfma_f32_32x32x16_f16 v[50:65], v[118:121], v[174:177], v[50:65]
	v_addc_co_u32_e32 v213, vcc, 0, v181, vcc
	v_lshl_add_u64 v[214:215], v[180:181], 0, s[8:9]
	s_waitcnt lgkmcnt(2)
	v_mfma_f32_32x32x16_f16 v[34:49], v[118:121], v[170:173], v[34:49]
	global_load_dwordx4 v[118:121], v[180:181], off
	s_waitcnt vmcnt(15)
	v_mfma_f32_32x32x16_f16 v[18:33], v[98:101], v[174:177], v[18:33]
	v_mfma_f32_32x32x16_f16 v[2:17], v[98:101], v[170:173], v[2:17]
	global_load_dwordx4 v[98:101], v[212:213], off offset:-4096
	ds_read_b128 v[170:173], v210
	ds_read_b128 v[174:177], v210 offset:33280
	s_waitcnt vmcnt(15) lgkmcnt(3)
	v_mfma_f32_32x32x16_f16 v[50:65], v[114:117], v[166:169], v[50:65]
	s_waitcnt lgkmcnt(2)
	v_mfma_f32_32x32x16_f16 v[34:49], v[114:117], v[162:165], v[34:49]
	global_load_dwordx4 v[114:117], v[180:181], off offset:1024
	s_waitcnt vmcnt(15)
	v_mfma_f32_32x32x16_f16 v[18:33], v[102:105], v[166:169], v[18:33]
	v_mfma_f32_32x32x16_f16 v[2:17], v[102:105], v[162:165], v[2:17]
	global_load_dwordx4 v[102:105], v[214:215], off offset:1024
	ds_read_b128 v[162:165], v210 offset:32
	ds_read_b128 v[166:169], v210 offset:33312
	s_waitcnt vmcnt(15) lgkmcnt(3)
	v_mfma_f32_32x32x16_f16 v[50:65], v[122:125], v[170:173], v[50:65]
	s_waitcnt lgkmcnt(2)
	v_mfma_f32_32x32x16_f16 v[34:49], v[122:125], v[174:177], v[34:49]
	global_load_dwordx4 v[122:125], v[180:181], off offset:2048
	s_waitcnt vmcnt(15)
	v_mfma_f32_32x32x16_f16 v[18:33], v[106:109], v[170:173], v[18:33]
	v_mfma_f32_32x32x16_f16 v[2:17], v[106:109], v[174:177], v[2:17]
	global_load_dwordx4 v[106:109], v[214:215], off offset:2048
	ds_read_b128 v[170:173], v210 offset:64
	ds_read_b128 v[174:177], v210 offset:33344
	s_waitcnt vmcnt(15) lgkmcnt(3)
	v_mfma_f32_32x32x16_f16 v[50:65], v[126:129], v[162:165], v[50:65]
	s_waitcnt lgkmcnt(2)
	v_mfma_f32_32x32x16_f16 v[34:49], v[126:129], v[166:169], v[34:49]
	global_load_dwordx4 v[126:129], v[180:181], off offset:3072
	s_waitcnt vmcnt(15)
	v_mfma_f32_32x32x16_f16 v[18:33], v[110:113], v[162:165], v[18:33]
	v_mfma_f32_32x32x16_f16 v[2:17], v[110:113], v[166:169], v[2:17]
	global_load_dwordx4 v[110:113], v[214:215], off offset:3072
	ds_read_b128 v[162:165], v210 offset:96
	ds_read_b128 v[166:169], v210 offset:33376
	s_waitcnt vmcnt(15) lgkmcnt(3)
	v_mfma_f32_32x32x16_f16 v[50:65], v[146:149], v[170:173], v[50:65]
	v_lshl_add_u64 v[214:215], v[180:181], 0, s[12:13]
	s_waitcnt lgkmcnt(2)
	v_mfma_f32_32x32x16_f16 v[34:49], v[146:149], v[174:177], v[34:49]
	v_add_co_u32_e32 v146, vcc, s3, v180
	s_nop 1
	v_addc_co_u32_e32 v147, vcc, 0, v181, vcc
	s_waitcnt vmcnt(14)
	v_mfma_f32_32x32x16_f16 v[18:33], v[134:137], v[170:173], v[18:33]
	v_mfma_f32_32x32x16_f16 v[2:17], v[134:137], v[174:177], v[2:17]
	global_load_dwordx4 v[146:149], v[146:147], off
	s_nop 0
	global_load_dwordx4 v[134:137], v[212:213], off
	ds_read_b128 v[170:173], v210 offset:128
	ds_read_b128 v[174:177], v210 offset:33408
	v_lshl_add_u64 v[212:213], v[180:181], 0, s[10:11]
	s_waitcnt vmcnt(15) lgkmcnt(3)
	v_mfma_f32_32x32x16_f16 v[50:65], v[142:145], v[162:165], v[50:65]
	s_waitcnt lgkmcnt(2)
	v_mfma_f32_32x32x16_f16 v[34:49], v[142:145], v[166:169], v[34:49]
	s_waitcnt vmcnt(14)
	v_mfma_f32_32x32x16_f16 v[18:33], v[130:133], v[162:165], v[18:33]
	v_mfma_f32_32x32x16_f16 v[2:17], v[130:133], v[166:169], v[2:17]
	global_load_dwordx4 v[142:145], v[212:213], off offset:1024
	global_load_dwordx4 v[130:133], v[214:215], off offset:1024
	ds_read_b128 v[162:165], v210 offset:160
	ds_read_b128 v[166:169], v210 offset:33440
	s_waitcnt vmcnt(15) lgkmcnt(3)
	v_mfma_f32_32x32x16_f16 v[50:65], v[150:153], v[170:173], v[50:65]
	s_waitcnt lgkmcnt(2)
	v_mfma_f32_32x32x16_f16 v[34:49], v[150:153], v[174:177], v[34:49]
	s_waitcnt vmcnt(14)
	v_mfma_f32_32x32x16_f16 v[18:33], v[138:141], v[170:173], v[18:33]
	v_mfma_f32_32x32x16_f16 v[2:17], v[138:141], v[174:177], v[2:17]
	global_load_dwordx4 v[150:153], v[212:213], off offset:2048
	global_load_dwordx4 v[138:141], v[214:215], off offset:2048
	ds_read_b128 v[174:177], v210 offset:192
	ds_read_b128 v[170:173], v210 offset:33472
	s_waitcnt vmcnt(15) lgkmcnt(3)
	v_mfma_f32_32x32x16_f16 v[50:65], v[158:161], v[162:165], v[50:65]
	s_waitcnt lgkmcnt(2)
	v_mfma_f32_32x32x16_f16 v[34:49], v[158:161], v[166:169], v[34:49]
	s_waitcnt vmcnt(14)
	v_mfma_f32_32x32x16_f16 v[18:33], v[154:157], v[162:165], v[18:33]
	v_mfma_f32_32x32x16_f16 v[2:17], v[154:157], v[166:169], v[2:17]
	global_load_dwordx4 v[158:161], v[212:213], off offset:3072
	global_load_dwordx4 v[154:157], v[214:215], off offset:3072
	ds_read_b128 v[166:169], v210 offset:224
	ds_read_b128 v[162:165], v210 offset:33504
	s_add_i32 s14, s14, 8
	v_add_u32_e32 v210, 0x100, v210
	s_cmp_lt_u32 s14, 16
	v_lshl_add_u64 v[180:181], v[180:181], 0, s[6:7]
	s_cbranch_scc1 .LBB3_21
	s_waitcnt vmcnt(15) lgkmcnt(3)
	v_mfma_f32_32x32x16_f16 v[50:65], v[118:121], v[174:177], v[50:65]
	s_waitcnt lgkmcnt(2)
	v_mfma_f32_32x32x16_f16 v[34:49], v[118:121], v[170:173], v[34:49]
	v_lshlrev_b32_e32 v118, 15, v209
	v_mov_b32_e32 v119, 0
	v_lshl_add_u64 v[120:121], s[0:1], 0, v[118:119]
	v_lshlrev_b32_e32 v118, 1, v178
	s_waitcnt vmcnt(14)
	v_mfma_f32_32x32x16_f16 v[18:33], v[98:101], v[174:177], v[18:33]
	v_lshl_add_u64 v[174:175], v[120:121], 0, v[118:119]
	ds_read_b128 v[118:121], v210
	ds_read_b128 v[212:215], v210 offset:33280
	v_mfma_f32_32x32x16_f16 v[2:17], v[98:101], v[170:173], v[2:17]
	s_waitcnt vmcnt(13) lgkmcnt(3)
	v_mfma_f32_32x32x16_f16 v[50:65], v[114:117], v[166:169], v[50:65]
	s_waitcnt lgkmcnt(2)
	v_mfma_f32_32x32x16_f16 v[34:49], v[114:117], v[162:165], v[34:49]
	ds_read_b128 v[98:101], v210 offset:32
	ds_read_b128 v[114:117], v210 offset:33312
	s_waitcnt vmcnt(12)
	v_mfma_f32_32x32x16_f16 v[18:33], v[102:105], v[166:169], v[18:33]
	v_mfma_f32_32x32x16_f16 v[2:17], v[102:105], v[162:165], v[2:17]
	s_waitcnt vmcnt(11) lgkmcnt(3)
	v_mfma_f32_32x32x16_f16 v[50:65], v[122:125], v[118:121], v[50:65]
	s_waitcnt lgkmcnt(2)
	v_mfma_f32_32x32x16_f16 v[34:49], v[122:125], v[212:215], v[34:49]
	s_waitcnt vmcnt(10)
	v_mfma_f32_32x32x16_f16 v[18:33], v[106:109], v[118:121], v[18:33]
	ds_read_b128 v[102:105], v210 offset:64
	ds_read_b128 v[118:121], v210 offset:33344
	v_mfma_f32_32x32x16_f16 v[2:17], v[106:109], v[212:215], v[2:17]
	s_waitcnt vmcnt(9) lgkmcnt(3)
	v_mfma_f32_32x32x16_f16 v[50:65], v[126:129], v[98:101], v[50:65]
	s_waitcnt lgkmcnt(2)
	v_mfma_f32_32x32x16_f16 v[34:49], v[126:129], v[114:117], v[34:49]
	s_waitcnt vmcnt(8)
	v_mfma_f32_32x32x16_f16 v[18:33], v[110:113], v[98:101], v[18:33]
	ds_read_b128 v[98:101], v210 offset:96
	ds_read_b128 v[106:109], v210 offset:33376
	v_mfma_f32_32x32x16_f16 v[2:17], v[110:113], v[114:117], v[2:17]
	s_waitcnt vmcnt(7) lgkmcnt(3)
	v_mfma_f32_32x32x16_f16 v[50:65], v[146:149], v[102:105], v[50:65]
	s_waitcnt lgkmcnt(2)
	v_mfma_f32_32x32x16_f16 v[34:49], v[146:149], v[118:121], v[34:49]
	s_waitcnt vmcnt(6)
	v_mfma_f32_32x32x16_f16 v[18:33], v[134:137], v[102:105], v[18:33]
	ds_read_b128 v[102:105], v210 offset:128
	ds_read_b128 v[110:113], v210 offset:33408
	v_mfma_f32_32x32x16_f16 v[2:17], v[134:137], v[118:121], v[2:17]
	s_waitcnt vmcnt(5) lgkmcnt(3)
	v_mfma_f32_32x32x16_f16 v[50:65], v[142:145], v[98:101], v[50:65]
	s_waitcnt lgkmcnt(2)
	v_mfma_f32_32x32x16_f16 v[34:49], v[142:145], v[106:109], v[34:49]
	s_waitcnt vmcnt(4)
	v_mfma_f32_32x32x16_f16 v[18:33], v[130:133], v[98:101], v[18:33]
	ds_read_b128 v[98:101], v210 offset:160
	ds_read_b128 v[114:117], v210 offset:33440
	v_mfma_f32_32x32x16_f16 v[2:17], v[130:133], v[106:109], v[2:17]
	s_waitcnt vmcnt(3) lgkmcnt(3)
	v_mfma_f32_32x32x16_f16 v[50:65], v[150:153], v[102:105], v[50:65]
	s_waitcnt lgkmcnt(2)
	v_mfma_f32_32x32x16_f16 v[34:49], v[150:153], v[110:113], v[34:49]
	s_waitcnt vmcnt(2)
	v_mfma_f32_32x32x16_f16 v[18:33], v[138:141], v[102:105], v[18:33]
	v_mfma_f32_32x32x16_f16 v[2:17], v[138:141], v[110:113], v[2:17]
	s_waitcnt vmcnt(1) lgkmcnt(1)
	v_mfma_f32_32x32x16_f16 v[50:65], v[158:161], v[98:101], v[50:65]
	s_waitcnt lgkmcnt(0)
	v_mfma_f32_32x32x16_f16 v[34:49], v[158:161], v[114:117], v[34:49]
	s_waitcnt vmcnt(0)
	v_mfma_f32_32x32x16_f16 v[18:33], v[154:157], v[98:101], v[18:33]
	v_mfma_f32_32x32x16_f16 v[2:17], v[154:157], v[114:117], v[2:17]
	v_readfirstlane_b32 s0, v209
	s_lshl_b32 s0, s0, 13
	s_cmp_lg_u32 0, -1
	s_cselect_b32 s1, 0, 0
	s_add_i32 s3, s1, s0
	s_mov_b64 s[0:1], 0x2000
	s_add_i32 s6, s3, 0x13400
	v_lshl_add_u64 v[98:99], v[174:175], 0, s[0:1]
	s_mov_b32 s7, m0
	s_mov_b32 m0, s6
	s_nop 0
	global_load_lds_dwordx4 v[98:99], off
	s_mov_b32 m0, s7
	s_mov_b64 s[6:7], 0x2400
	v_lshl_add_u64 v[98:99], v[174:175], 0, s[6:7]
	s_add_i32 s6, s3, 0x13800
	s_mov_b32 s7, m0
	s_mov_b32 m0, s6
	s_nop 0
	global_load_lds_dwordx4 v[98:99], off
	s_mov_b32 m0, s7
	s_mov_b64 s[6:7], 0x2800
	v_lshl_add_u64 v[98:99], v[174:175], 0, s[6:7]
	s_add_i32 s6, s3, 0x13c00
	s_mov_b32 s7, m0
	s_mov_b32 m0, s6
	s_nop 0
	global_load_lds_dwordx4 v[98:99], off
	s_mov_b32 m0, s7
	s_mov_b64 s[6:7], 0x2c00
	v_lshl_add_u64 v[98:99], v[174:175], 0, s[6:7]
	s_add_i32 s6, s3, 0x14000
	s_mov_b32 s7, m0
	s_mov_b32 m0, s6
	s_nop 0
	global_load_lds_dwordx4 v[98:99], off
	s_mov_b32 m0, s7
	s_mov_b64 s[6:7], 0x3000
	v_lshl_add_u64 v[98:99], v[174:175], 0, s[6:7]
	s_add_i32 s6, s3, 0x14400
	s_mov_b32 s7, m0
	s_mov_b32 m0, s6
	s_nop 0
	global_load_lds_dwordx4 v[98:99], off
	s_mov_b32 m0, s7
	s_mov_b64 s[6:7], 0x3400
	v_lshl_add_u64 v[98:99], v[174:175], 0, s[6:7]
	s_add_i32 s6, s3, 0x14800
	s_mov_b32 s7, m0
	s_mov_b32 m0, s6
	s_nop 0
	global_load_lds_dwordx4 v[98:99], off
	s_mov_b32 m0, s7
	s_mov_b64 s[6:7], 0x3800
	v_lshl_add_u64 v[98:99], v[174:175], 0, s[6:7]
	s_add_i32 s6, s3, 0x14c00
	s_mov_b32 s7, m0
	s_mov_b32 m0, s6
	s_nop 0
	global_load_lds_dwordx4 v[98:99], off
	s_mov_b32 m0, s7
	s_mov_b64 s[6:7], 0x3c00
	v_lshl_add_u64 v[98:99], v[174:175], 0, s[6:7]
	s_add_i32 s3, s3, 0x15000
	s_mov_b32 s6, m0
	s_mov_b32 m0, s3
	s_nop 0
	global_load_lds_dwordx4 v[98:99], off
	s_mov_b32 m0, s6
	global_load_dwordx4 v[126:129], v[174:175], off
	s_mov_b32 s3, 0
	global_load_dwordx4 v[122:125], v[174:175], off offset:1024
	global_load_dwordx4 v[118:121], v[174:175], off offset:2048
	global_load_dwordx4 v[114:117], v[174:175], off offset:3072
	s_movk_i32 s9, 0x1000
	v_add_co_u32_e32 v98, vcc, s9, v174
	s_nop 1
	v_addc_co_u32_e32 v99, vcc, 0, v175, vcc
	global_load_dwordx4 v[110:113], v[98:99], off
	global_load_dwordx4 v[106:109], v[98:99], off offset:1024
	global_load_dwordx4 v[102:105], v[98:99], off offset:2048
	s_nop 0
	global_load_dwordx4 v[98:101], v[98:99], off offset:3072
	v_and_b32_e32 v151, 0x1c0, v0
	v_lshlrev_b32_e32 v130, 2, v151
	s_add_i32 s6, 0, 0x11800
	v_lshlrev_b32_e32 v150, 4, v208
	v_add3_u32 v156, s6, v130, v150
	ds_read_b128 v[130:133], v156
	ds_read_b128 v[152:155], v156 offset:32
	s_waitcnt lgkmcnt(1)
	v_add_f32_e64 v148, v130, v50
	v_add_f32_e64 v149, v131, v51
	s_nop 0
	v_add_f32_e32 v51, 0, v148
	v_mul_f32_e32 v50, v149, v149
	v_add_f32_e32 v134, v51, v149
	v_add_f32_e64 v146, v132, v52
	v_add_f32_e64 v147, v133, v53
	v_fma_f32 v51, v149, v149, v50
	v_fma_f32 v50, v148, v148, v50
	v_add_f32_e32 v52, v134, v146
	v_add_f32_e64 v144, v130, v34
	v_add_f32_e64 v145, v131, v35
	v_fma_f32 v50, v146, v146, v50
	v_fma_f32 v51, v147, v147, v51
	v_add_f32_e32 v53, v52, v147
	v_mul_f32_e32 v52, v147, v147
	v_add_f32_e32 v34, 0, v144
	v_add_f32_e64 v50, v52, v50
	v_add_f32_e64 v51, v52, v51
	v_add_f32_e32 v52, v34, v145
	v_mul_f32_e32 v34, v145, v145
	v_add_f32_e64 v142, v132, v36
	v_add_f32_e64 v143, v133, v37
	v_fma_f32 v35, v145, v145, v34
	v_fma_f32 v34, v144, v144, v34
	v_add_f32_e32 v36, v52, v142
	s_waitcnt lgkmcnt(0)
	v_add_f32_e64 v140, v152, v54
	v_add_f32_e64 v141, v153, v55
	v_fma_f32 v34, v142, v142, v34
	v_fma_f32 v35, v143, v143, v35
	v_add_f32_e32 v52, v36, v143
	v_mul_f32_e32 v36, v143, v143
	v_add_f32_e32 v53, v53, v140
	v_add_f32_e64 v34, v36, v34
	v_add_f32_e64 v35, v36, v35
	v_fma_f32 v36, v140, v140, v50
	v_fma_f32 v37, v141, v141, v51
	v_add_f32_e32 v51, v53, v141
	v_mul_f32_e32 v50, v141, v141
	v_add_f32_e64 v138, v154, v56
	v_add_f32_e64 v139, v155, v57
	v_add_f32_e64 v36, v50, v36
	v_add_f32_e64 v37, v50, v37
	v_add_f32_e32 v50, v51, v138
	v_fma_f32 v36, v138, v138, v36
	v_fma_f32 v37, v139, v139, v37
	v_add_f32_e32 v54, v50, v139
	v_mul_f32_e32 v50, v139, v139
	v_add_f32_e64 v136, v152, v38
	v_add_f32_e64 v137, v153, v39
	v_add_f32_e64 v51, v50, v37
	v_add_f32_e64 v50, v50, v36
	v_add_f32_e32 v36, v52, v136
	v_fma_f32 v34, v136, v136, v34
	v_fma_f32 v35, v137, v137, v35
	v_add_f32_e32 v37, v36, v137
	v_mul_f32_e32 v36, v137, v137
	v_add_f32_e64 v34, v36, v34
	v_add_f32_e64 v35, v36, v35
	v_add_f32_e64 v132, v154, v40
	v_add_f32_e64 v133, v155, v41
	s_nop 0
	v_add_f32_e32 v40, v37, v132
	v_fma_f32 v38, v132, v132, v34
	v_fma_f32 v39, v133, v133, v35
	ds_read_b128 v[34:37], v156 offset:64
	v_add_f32_e32 v55, v40, v133
	v_mul_f32_e32 v40, v133, v133
	v_add_f32_e64 v52, v40, v38
	v_add_f32_e64 v53, v40, v39
	ds_read_b128 v[38:41], v156 offset:96
	s_waitcnt lgkmcnt(1)
	v_add_f32_e64 v134, v34, v58
	v_add_f32_e64 v135, v35, v59
	v_add_f32_e64 v130, v36, v60
	v_add_f32_e64 v131, v37, v61
	v_add_f32_e32 v54, v54, v134
	v_add_f32_e64 v60, v34, v42
	v_add_f32_e64 v61, v35, v43
	v_fma_f32 v50, v134, v134, v50
	v_fma_f32 v51, v135, v135, v51
	v_add_f32_e32 v56, v54, v135
	v_mul_f32_e32 v54, v135, v135
	v_add_f32_e32 v42, v55, v60
	v_add_f32_e64 v50, v54, v50
	v_add_f32_e64 v51, v54, v51
	v_add_f32_e32 v54, v56, v130
	v_fma_f32 v34, v60, v60, v52
	v_fma_f32 v35, v61, v61, v53
	v_add_f32_e32 v43, v42, v61
	v_mul_f32_e32 v42, v61, v61
	v_add_f32_e64 v58, v36, v44
	v_add_f32_e64 v59, v37, v45
	v_fma_f32 v50, v130, v130, v50
	v_fma_f32 v51, v131, v131, v51
	v_add_f32_e32 v152, v54, v131
	v_mul_f32_e32 v54, v131, v131
	v_add_f32_e64 v34, v42, v34
	v_add_f32_e64 v35, v42, v35
	v_add_f32_e32 v36, v43, v58
	s_waitcnt lgkmcnt(0)
	v_add_f32_e64 v56, v38, v62
	v_add_f32_e64 v57, v39, v63
	v_add_f32_e64 v50, v54, v50
	v_add_f32_e64 v51, v54, v51
	v_fma_f32 v34, v58, v58, v34
	v_fma_f32 v35, v59, v59, v35
	v_add_f32_e32 v44, v36, v59
	v_mul_f32_e32 v36, v59, v59
	v_add_f32_e32 v42, v152, v56
	v_add_f32_e64 v34, v36, v34
	v_add_f32_e64 v35, v36, v35
	v_fma_f32 v36, v56, v56, v50
	v_fma_f32 v37, v57, v57, v51
	v_add_f32_e32 v43, v42, v57
	v_mul_f32_e32 v42, v57, v57
	v_add_f32_e64 v54, v40, v64
	v_add_f32_e64 v55, v41, v65
	v_add_f32_e64 v36, v42, v36
	v_add_f32_e64 v37, v42, v37
	v_add_f32_e32 v42, v43, v54
	v_fma_f32 v36, v54, v54, v36
	v_fma_f32 v37, v55, v55, v37
	v_add_f32_e32 v45, v42, v55
	v_mul_f32_e32 v42, v55, v55
	v_add_f32_e64 v52, v38, v46
	v_add_f32_e64 v53, v39, v47
	v_add_f32_e64 v43, v42, v37
	v_add_f32_e64 v42, v42, v36
	v_add_f32_e32 v36, v44, v52
	v_fma_f32 v34, v52, v52, v34
	v_fma_f32 v35, v53, v53, v35
	v_add_f32_e32 v37, v36, v53
	v_mul_f32_e32 v36, v53, v53
	v_add_f32_e64 v34, v36, v34
	v_add_f32_e64 v35, v36, v35
	v_add_f32_e64 v50, v40, v48
	v_add_f32_e64 v51, v41, v49
	ds_read_b128 v[62:65], v156 offset:160
	v_add_f32_e32 v40, v37, v50
	v_fma_f32 v38, v50, v50, v34
	v_fma_f32 v39, v51, v51, v35
	ds_read_b128 v[34:37], v156 offset:128
	v_add_f32_e32 v41, v40, v51
	v_mul_f32_e32 v40, v51, v51
	v_add_f32_e64 v38, v40, v38
	v_add_f32_e64 v39, v40, v39
	s_waitcnt lgkmcnt(0)
	v_add_f32_e64 v48, v34, v18
	v_add_f32_e64 v49, v35, v19
	s_nop 0
	v_add_f32_e32 v40, v45, v48
	v_fma_f32 v18, v48, v48, v42
	v_fma_f32 v19, v49, v49, v43
	v_add_f32_e32 v42, v40, v49
	v_add_f32_e64 v46, v36, v20
	v_add_f32_e64 v47, v37, v21
	v_add_f32_e64 v44, v34, v2
	v_add_f32_e64 v45, v35, v3
	v_add_f32_e32 v20, v42, v46
	v_mul_f32_e32 v40, v49, v49
	v_add_f32_e32 v21, v20, v47
	v_add_f32_e32 v20, v41, v44
	v_add_f32_e64 v18, v40, v18
	v_add_f32_e64 v19, v40, v19
	v_fma_f32 v2, v44, v44, v38
	v_fma_f32 v3, v45, v45, v39
	v_add_f32_e32 v34, v20, v45
	v_mul_f32_e32 v20, v45, v45
	v_add_f32_e64 v42, v36, v4
	v_add_f32_e64 v43, v37, v5
	v_add_f32_e64 v40, v62, v22
	v_add_f32_e64 v41, v63, v23
	v_fma_f32 v18, v46, v46, v18
	v_fma_f32 v19, v47, v47, v19
	v_add_f32_e64 v2, v20, v2
	v_add_f32_e64 v3, v20, v3
	v_add_f32_e32 v4, v34, v42
	v_add_f32_e32 v21, v21, v40
	v_mul_f32_e32 v20, v47, v47
	v_add_f32_e32 v34, v4, v43
	v_mov_b32_e32 v4, v40
	v_mov_b32_e32 v5, v47
	v_add_f32_e64 v18, v20, v18
	v_add_f32_e64 v19, v20, v19
	v_fma_f32 v4, v4, v4, v18
	v_fma_f32 v5, v5, v5, v19
	v_add_f32_e32 v18, v21, v41
	v_add_f32_e64 v38, v64, v24
	v_add_f32_e64 v39, v65, v25
	v_mul_f32_e32 v20, v41, v41
	v_add_f32_e32 v21, v18, v38
	v_fma_f32 v2, v42, v42, v2
	v_fma_f32 v3, v43, v43, v3
	v_mov_b32_e32 v18, v38
	v_mov_b32_e32 v19, v41
	v_add_f32_e64 v4, v20, v4
	v_add_f32_e64 v5, v20, v5
	v_add_f32_e64 v36, v62, v6
	v_add_f32_e64 v37, v63, v7
	v_mul_f32_e32 v6, v43, v43
	v_fma_f32 v18, v18, v18, v4
	v_fma_f32 v19, v19, v19, v5
	v_add_f32_e32 v20, v34, v36
	v_mov_b32_e32 v4, v36
	v_mov_b32_e32 v5, v43
	v_add_f32_e64 v2, v6, v2
	v_add_f32_e64 v3, v6, v3
	v_fma_f32 v6, v4, v4, v2
	v_fma_f32 v7, v5, v5, v3
	v_add_f32_e32 v2, v20, v37
	v_add_f32_e64 v34, v64, v8
	v_add_f32_e64 v35, v65, v9
	v_add_f32_e32 v21, v21, v39
	v_add_f32_e32 v22, v2, v34
	ds_read_b128 v[2:5], v156 offset:192
	ds_read_b128 v[62:65], v156 offset:224
	v_mul_f32_e32 v20, v37, v37
	v_mov_b32_e32 v8, v34
	v_mov_b32_e32 v9, v37
	s_waitcnt lgkmcnt(1)
	v_add_f32_e64 v26, v2, v26
	v_add_f32_e64 v27, v3, v27
	v_add_f32_e64 v6, v20, v6
	v_add_f32_e64 v7, v20, v7
	v_add_f32_e32 v21, v21, v26
	v_mul_f32_e32 v20, v39, v39
	v_fma_f32 v6, v8, v8, v6
	v_fma_f32 v7, v9, v9, v7
	v_mov_b32_e32 v8, v26
	v_mov_b32_e32 v9, v39
	v_add_f32_e64 v18, v20, v18
	v_add_f32_e64 v19, v20, v19
	v_fma_f32 v8, v8, v8, v18
	v_fma_f32 v9, v9, v9, v19
	v_add_f32_e32 v18, v21, v27
	v_add_f32_e64 v24, v4, v28
	v_add_f32_e64 v25, v5, v29
	v_mul_f32_e32 v20, v27, v27
	v_add_f32_e32 v21, v18, v24
	v_add_f32_e32 v152, v22, v35
	v_mov_b32_e32 v18, v24
	v_mov_b32_e32 v19, v27
	v_add_f32_e64 v8, v20, v8
	v_add_f32_e64 v9, v20, v9
	v_add_f32_e32 v28, v21, v25
	v_add_f32_e64 v20, v2, v10
	v_add_f32_e64 v21, v3, v11
	v_fma_f32 v22, v18, v18, v8
	v_fma_f32 v23, v19, v19, v9
	v_add_f32_e32 v9, v152, v20
	v_mul_f32_e32 v8, v35, v35
	v_mov_b32_e32 v2, v20
	v_mov_b32_e32 v3, v35
	v_add_f32_e64 v6, v8, v6
	v_add_f32_e64 v7, v8, v7
	v_fma_f32 v2, v2, v2, v6
	v_fma_f32 v3, v3, v3, v7
	v_add_f32_e32 v6, v9, v21
	v_add_f32_e64 v18, v4, v12
	v_add_f32_e64 v19, v5, v13
	v_mov_b32_e32 v5, v21
	v_add_f32_e32 v7, v6, v18
	v_mul_f32_e32 v6, v21, v21
	v_mov_b32_e32 v4, v18
	v_add_f32_e64 v2, v6, v2
	v_add_f32_e64 v3, v6, v3
	s_waitcnt lgkmcnt(0)
	v_add_f32_e64 v8, v62, v30
	v_add_f32_e64 v9, v63, v31
	v_mul_f32_e32 v6, v25, v25
	v_fma_f32 v2, v4, v4, v2
	v_fma_f32 v3, v5, v5, v3
	v_add_f32_e32 v29, v7, v19
	v_mov_b32_e32 v4, v8
	v_mov_b32_e32 v5, v25
	v_add_f32_e64 v7, v6, v23
	v_add_f32_e64 v6, v6, v22
	v_fma_f32 v4, v4, v4, v6
	v_fma_f32 v5, v5, v5, v7
	v_add_f32_e64 v6, v64, v32
	v_add_f32_e64 v7, v65, v33
	v_mul_f32_e32 v22, v9, v9
	v_add_f32_e32 v10, v28, v8
	v_mov_b32_e32 v12, v6
	v_mov_b32_e32 v13, v9
	v_add_f32_e64 v4, v22, v4
	v_add_f32_e64 v5, v22, v5
	v_add_f32_e32 v10, v10, v9
	v_fma_f32 v4, v12, v12, v4
	v_fma_f32 v5, v13, v13, v5
	v_mul_f32_e64 v12, v6, v6
	v_mul_f32_e64 v13, v7, v7
	v_add_f32_e32 v10, v10, v6
	v_mov_b32_e32 v11, v13
	v_pk_mov_b32 v[4:5], v[6:7], v[4:5] op_sel:[1,0]
	v_mov_b32_e32 v13, v19
	v_add_f32_e64 v10, v10, v4
	v_add_f32_e64 v11, v11, v5
	v_add_f32_e64 v4, v62, v14
	v_add_f32_e64 v5, v63, v15
	v_mul_f32_e32 v14, v19, v19
	v_add_f32_e32 v15, v29, v4
	v_mov_b32_e32 v12, v4
	v_add_f32_e64 v2, v14, v2
	v_add_f32_e64 v3, v14, v3
	v_fma_f32 v12, v12, v12, v2
	v_fma_f32 v13, v13, v13, v3
	v_add_f32_e64 v2, v64, v16
	v_add_f32_e64 v3, v65, v17
	v_mul_f32_e32 v22, v5, v5
	v_mov_b32_e32 v16, v2
	v_mov_b32_e32 v17, v5
	v_add_f32_e64 v12, v22, v12
	v_add_f32_e64 v13, v22, v13
	v_add_f32_e32 v14, v15, v5
	v_fma_f32 v12, v16, v16, v12
	v_fma_f32 v13, v17, v17, v13
	v_mul_f32_e64 v16, v2, v2
	v_mul_f32_e64 v17, v3, v3
	v_add_f32_e32 v14, v14, v2
	v_mov_b32_e32 v15, v17
	v_pk_mov_b32 v[12:13], v[2:3], v[12:13] op_sel:[1,0]
	s_nop 0
	v_add_f32_e64 v12, v14, v12
	v_add_f32_e64 v13, v15, v13
	v_mbcnt_lo_u32_b32 v14, -1, 0
	v_mbcnt_hi_u32_b32 v14, -1, v14
	v_and_b32_e32 v16, 64, v14
	v_xor_b32_e32 v15, 32, v14
	v_add_u32_e32 v16, 64, v16
	v_cmp_lt_i32_e32 vcc, v15, v16
	s_nop 1
	v_cndmask_b32_e32 v14, v14, v15, vcc
	v_lshlrev_b32_e32 v17, 2, v14
	ds_bpermute_b32 v14, v17, v10
	ds_bpermute_b32 v15, v17, v11
	ds_bpermute_b32 v16, v17, v12
	ds_bpermute_b32 v17, v17, v13
	v_cmp_gt_u32_e32 vcc, 32, v206
	s_and_saveexec_b64 s[6:7], vcc
	s_cbranch_execz .LBB3_24
	s_waitcnt lgkmcnt(2)
	v_add_f32_e64 v10, v10, v14
	v_add_f32_e64 v11, v11, v15
	v_and_b32_e32 v14, 0x1df, v0
	s_add_i32 s8, 0, 0x10400
	v_lshl_add_u32 v14, v14, 3, s8
	ds_write_b64 v14, v[10:11]
	v_mov_b32_e32 v10, 0x100
	v_lshl_or_b32 v10, v0, 3, v10
	s_waitcnt lgkmcnt(1)
	v_add_f32_e64 v12, v12, v16
	v_add_f32_e64 v13, v13, v17
	v_add_u32_e32 v10, s8, v10
	ds_write_b64 v10, v[12:13]
